# layer-0 MoE combine + fused LN1: the row's loads issued up front in three batches into their own registers (hipcc had ~17 dependent load/wait/compute/store groups per row); plus the diff-combine load
# speedup vs baseline: 1.0087x; 1.0004x over previous
; __device__ __forceinline__ unsigned pk2(float lo, float hi) { unsigned r; asm volatile("v_cvt_pk_bf16_f32 %0, %1, %2" : "=v"(r) : "v"(lo), "v"(hi)); return r; }
; template <bool FINAL>
; __device__ __forceinline__ void ph_moe_combine(const P& p, int l, int row0, int gw, int nw, int lane) {
;   for (int r = row0 + gw; r < NTOK; r += nw) {
;     const float* gt = WSP(float, WS_MOD) + ((size_t)l * 2 + (r < CTXL ? 1 : 0)) * MODW + 5 * DM;
;     const int s0 = WSP(int, WS_SLOT)[r * 2], s1 = WSP(int, WS_SLOT)[r * 2 + 1]; const float w0 = WSP(float, WS_EW)[r * 2], w1 = WSP(float, WS_EW)[r * 2 + 1];
;     const bf16_t* y0 = WSP(bf16_t, WS_YP) + (size_t)s0 * DM; const bf16_t* y1 = WSP(bf16_t, WS_YP) + (size_t)s1 * DM;
;     bf16_t* xr = WSP(bf16_t, WS_X) + (size_t)r * DM;
;     f32x4 v[8]; float ss = 0;
; #pragma unroll
;     for (int j = 0; j < 8; ++j) { const int c = (lane + 64 * j) * 4;
;       const u32x2 a = __builtin_nontemporal_load((const u32x2*)(y0 + c)), b = __builtin_nontemporal_load((const u32x2*)(y1 + c)); f32x4 xv = ldx4(xr + c); const f32x4 g = *(const f32x4*)(gt + c);
;       xv.x += g.x * (w0 * __uint_as_float(a.x << 16) + w1 * __uint_as_float(b.x << 16));
;       xv.y += g.y * (w0 * __uint_as_float(a.x & 0xffff0000u) + w1 * __uint_as_float(b.x & 0xffff0000u));
;       xv.z += g.z * (w0 * __uint_as_float(a.y << 16) + w1 * __uint_as_float(b.y << 16));
;       xv.w += g.w * (w0 * __uint_as_float(a.y & 0xffff0000u) + w1 * __uint_as_float(b.y & 0xffff0000u));
;       v[j] = xv; ss += xv.x * xv.x + xv.y * xv.y + xv.z * xv.z + xv.w * xv.w;
;       if (!FINAL) stx4(xr + c, xv); }
;     if (!FINAL) {
;       const float rs = rsqrtf(wave_sum(ss) * (1.f / DM) + EPS);
;       const float* g1 = p.n1 + (l + 1) * DM; const float* md = WSP(float, WS_MOD) + ((size_t)(l + 1) * 2 + (r < CTXL ? 1 : 0)) * MODW;
;       bf16_t* o = WSP(bf16_t, WS_HN) + (size_t)r * DM;
; #pragma unroll
;       for (int j = 0; j < 8; ++j) { const int c = (lane + 64 * j) * 4; const f32x4 gg = *(const f32x4*)(g1 + c), sh = *(const f32x4*)(md + c), sc = *(const f32x4*)(md + DM + c);
;         u32x2 w2; w2.x = pk2(v[j].x * rs * gg.x * (1.f + sc.x) + sh.x, v[j].y * rs * gg.y * (1.f + sc.y) + sh.y); w2.y = pk2(v[j].z * rs * gg.z * (1.f + sc.z) + sh.z, v[j].w * rs * gg.w * (1.f + sc.w) + sh.w);
;         *(u32x2*)(o + c) = w2; }
;     }
.LBB0_1421:
	s_cmpk_lt_i32 s14, 0x100
	s_cselect_b64 s[16:17], -1, 0
	s_mov_b32 s15, 0xfbe00000
	v_cndmask_b32_e64 v34, 0, 1, s[16:17]
	v_add_co_u32_e32 v30, vcc, s15, v12
	v_readfirstlane_b32 s15, v34
	s_or_b32 s16, s18, s15
	s_mul_i32 s23, s19, 0xc000
	s_mul_hi_u32 s17, s16, 0xc000
	s_mul_i32 s16, s16, 0xc000
	s_add_i32 s17, s17, s23
	s_add_u32 s16, s50, s16
	s_addc_u32 s17, s51, s17
	s_add_u32 s38, s16, 0x38e000
	s_addc_u32 s39, s17, 0
	s_ashr_i32 s23, s22, 31
	s_lshl_b64 s[34:35], s[22:23], 2
	s_add_u32 s16, s1, s34
	s_addc_u32 s17, s2, s35
	v_addc_co_u32_e32 v31, vcc, -1, v13, vcc
	global_load_dwordx2 v[64:65], v97, s[16:17]
	global_load_dwordx2 v[32:33], v[30:31], off offset:-3584
	s_add_i32 s30, s22, 1
	s_ashr_i32 s31, s30, 31
	s_add_u32 s16, s3, s34
	s_addc_u32 s17, s6, s35
	s_lshl_b64 s[30:31], s[30:31], 2
	global_load_dword v48, v97, s[16:17]
	s_add_u32 s16, s3, s30
	v_lshl_add_u64 v[36:37], s[38:39], 0, v[14:15]
	s_addc_u32 s17, s6, s31
	global_load_dwordx4 v[60:63], v[36:37], off
	global_load_dword v49, v97, s[16:17]
	v_lshl_add_u64 v[34:35], s[38:39], 0, v[16:17]
	v_lshl_add_u64 v[38:39], s[38:39], 0, v[18:19]
	v_lshl_add_u64 v[40:41], s[38:39], 0, v[20:21]
	v_lshl_add_u64 v[42:43], s[38:39], 0, v[22:23]
	v_lshl_add_u64 v[44:45], s[38:39], 0, v[24:25]
	v_lshl_add_u64 v[46:47], s[38:39], 0, v[26:27]
	v_lshl_add_u64 v[52:53], s[38:39], 0, v[28:29]
	s_or_b32 s15, s4, s15
	s_mul_hi_u32 s16, s15, 0xc000
	s_mul_i32 s15, s15, 0xc000
	s_add_i32 s16, s16, s5
	s_add_u32 s34, s7, s15
	s_addc_u32 s35, s9, s16
	s_add_u32 s38, s34, 0x2000
	s_addc_u32 s39, s35, 0
	v_lshl_add_u64 v[36:37], s[34:35], 0, v[14:15]
	v_lshl_add_u64 v[56:57], s[38:39], 0, v[14:15]
	v_lshl_add_u64 v[54:55], s[38:39], 0, v[16:17]
	v_lshl_add_u64 v[50:51], s[38:39], 0, v[18:19]
	s_add_i32 s14, s14, s12
	s_add_i32 s22, s22, s13
	s_cmpk_lt_i32 s14, 0x2100
	global_load_dwordx2 v[100:101], v[30:31], off offset:-3072
	global_load_dwordx4 v[108:111], v[34:35], off
	global_load_dwordx2 v[106:107], v[30:31], off offset:-2560
	global_load_dwordx4 v[116:119], v[38:39], off
	global_load_dwordx2 v[120:121], v[30:31], off offset:-2048
	global_load_dwordx4 v[128:131], v[40:41], off
	global_load_dwordx2 v[126:127], v[30:31], off offset:-1536
	global_load_dwordx4 v[136:139], v[42:43], off
	global_load_dwordx2 v[140:141], v[30:31], off offset:-1024
	global_load_dwordx4 v[148:151], v[44:45], off
	global_load_dwordx2 v[146:147], v[30:31], off offset:-512
	global_load_dwordx4 v[156:159], v[46:47], off
	global_load_dwordx2 v[160:161], v[30:31], off
	global_load_dwordx4 v[168:171], v[52:53], off
	global_load_dwordx4 v[172:175], v[0:1], off
	global_load_dwordx4 v[180:183], v14, s[38:39]
	global_load_dwordx4 v[184:187], v14, s[34:35]
	global_load_dwordx4 v[188:191], v[0:1], off offset:1024
	global_load_dwordx4 v[192:195], v14, s[38:39] offset:1024
	global_load_dwordx4 v[196:199], v14, s[34:35] offset:1024
	global_load_dwordx4 v[200:203], v[0:1], off offset:2048
	global_load_dwordx4 v[204:207], v14, s[38:39] offset:2048
	global_load_dwordx4 v[208:211], v14, s[34:35] offset:2048
	global_load_dwordx4 v[212:215], v[0:1], off offset:3072
	global_load_dwordx4 v[224:227], v14, s[38:39] offset:3072
	global_load_dwordx4 v[228:231], v14, s[34:35] offset:3072
	global_load_dwordx4 v[232:235], v[2:3], off
	global_load_dwordx4 v[236:239], v22, s[38:39]
	global_load_dwordx4 v[240:243], v22, s[34:35]
	s_waitcnt vmcnt(0)
	v_ashrrev_i32_e32 v67, 31, v65
	v_mov_b32_e32 v66, v65
	v_lshlrev_b32_e32 v59, 16, v32
	v_and_b32_e32 v76, 0xffff0000, v32
	v_lshlrev_b32_e32 v77, 16, v33
	v_and_b32_e32 v78, 0xffff0000, v33
	v_ashrrev_i32_e32 v33, 31, v64
	v_mov_b32_e32 v32, v64
	v_lshlrev_b64 v[64:65], 12, v[66:67]
	v_lshlrev_b64 v[32:33], 12, v[32:33]
	v_lshl_add_u64 v[64:65], v[10:11], 0, v[64:65]
	v_lshl_add_u64 v[66:67], v[10:11], 0, v[32:33]
	global_load_dwordx2 v[32:33], v[64:65], off nt
	global_load_dwordx2 v[68:69], v[66:67], off nt
	global_load_dwordx2 v[102:103], v[64:65], off offset:512 nt
	global_load_dwordx2 v[104:105], v[66:67], off offset:512 nt
	global_load_dwordx2 v[112:113], v[64:65], off offset:1024 nt
	global_load_dwordx2 v[114:115], v[66:67], off offset:1024 nt
	global_load_dwordx2 v[122:123], v[64:65], off offset:1536 nt
	global_load_dwordx2 v[124:125], v[66:67], off offset:1536 nt
	global_load_dwordx2 v[132:133], v[64:65], off offset:2048 nt
	global_load_dwordx2 v[134:135], v[66:67], off offset:2048 nt
	global_load_dwordx2 v[142:143], v[64:65], off offset:2560 nt
	global_load_dwordx2 v[144:145], v[66:67], off offset:2560 nt
	global_load_dwordx2 v[152:153], v[64:65], off offset:3072 nt
	global_load_dwordx2 v[154:155], v[66:67], off offset:3072 nt
	global_load_dwordx2 v[162:163], v[64:65], off offset:3584 nt
	global_load_dwordx2 v[164:165], v[66:67], off offset:3584 nt
	s_waitcnt vmcnt(0)
; __device__ __forceinline__ f32x4 ldx4(const bf16_t* q) { const u32x2 w = *(const u32x2*)q; f32x4 r; r.x = __uint_as_float(w.x << 16); r.y = __uint_as_float(w.x & 0xffff0000u); r.z = __uint_as_float(w.y << 16); r.w = __uint_as_float(w.y & 0xffff0000u); return r; }
; __device__ __forceinline__ void stx4(bf16_t* q, const f32x4 v) { u32x2 w; w.x = pk2(v.x, v.y); w.y = pk2(v.z, v.w); *(u32x2*)q = w; }
; template <bool FINAL>
; __device__ __forceinline__ void ph_moe_combine(const P& p, int l, int row0, int gw, int nw, int lane) {
;     ...
;     for (int j = 0; j < 8; ++j) { const int c = (lane + 64 * j) * 4;
;       const u32x2 a = __builtin_nontemporal_load((const u32x2*)(y0 + c)), b = __builtin_nontemporal_load((const u32x2*)(y1 + c)); f32x4 xv = ldx4(xr + c); const f32x4 g = *(const f32x4*)(gt + c);
;       xv.x += g.x * (w0 * __uint_as_float(a.x << 16) + w1 * __uint_as_float(b.x << 16));
;       xv.y += g.y * (w0 * __uint_as_float(a.x & 0xffff0000u) + w1 * __uint_as_float(b.x & 0xffff0000u));
;       xv.z += g.z * (w0 * __uint_as_float(a.y << 16) + w1 * __uint_as_float(b.y << 16));
;       xv.w += g.w * (w0 * __uint_as_float(a.y & 0xffff0000u) + w1 * __uint_as_float(b.y & 0xffff0000u));
;       v[j] = xv; ss += xv.x * xv.x + xv.y * xv.y + xv.z * xv.z + xv.w * xv.w;
;       if (!FINAL) stx4(xr + c, xv); }
	v_lshlrev_b32_e32 v71, 16, v32
	v_lshlrev_b32_e32 v70, 16, v68
	v_and_b32_e32 v73, 0xffff0000, v32
	v_and_b32_e32 v72, 0xffff0000, v68
	v_lshlrev_b32_e32 v75, 16, v33
	v_lshlrev_b32_e32 v74, 16, v69
	v_and_b32_e32 v33, 0xffff0000, v33
	v_and_b32_e32 v32, 0xffff0000, v69
	v_pk_mul_f32 v[68:69], v[48:49], v[70:71]
	v_pk_mul_f32 v[70:71], v[48:49], v[72:73]
	v_pk_mul_f32 v[72:73], v[48:49], v[74:75]
	v_pk_mul_f32 v[32:33], v[48:49], v[32:33]
	v_add_f32_e32 v68, v68, v69
	v_add_f32_e32 v69, v70, v71
	v_add_f32_e32 v70, v72, v73
	v_add_f32_e32 v32, v32, v33
	v_fmac_f32_e32 v59, v60, v68
	v_fmac_f32_e32 v76, v61, v69
	v_fmac_f32_e32 v77, v62, v70
	v_fmac_f32_e32 v78, v63, v32
	v_cvt_pk_bf16_f32 v32, v59, v76
	v_cvt_pk_bf16_f32 v33, v77, v78
	v_mul_f32_e32 v74, v76, v76
	global_store_dwordx2 v[30:31], v[32:33], off offset:-3584
	s_nop 0
	v_fmac_f32_e32 v74, v59, v59
	v_fmac_f32_e32 v74, v77, v77
	v_fmac_f32_e32 v74, v78, v78
	v_lshlrev_b32_e32 v75, 16, v100
	v_and_b32_e32 v79, 0xffff0000, v100
	v_lshlrev_b32_e32 v80, 16, v101
	v_and_b32_e32 v81, 0xffff0000, v101
	v_lshlrev_b32_e32 v61, 16, v102
	v_lshlrev_b32_e32 v60, 16, v104
	v_and_b32_e32 v71, 0xffff0000, v102
	v_and_b32_e32 v70, 0xffff0000, v104
	v_lshlrev_b32_e32 v73, 16, v103
	v_lshlrev_b32_e32 v72, 16, v105
	v_and_b32_e32 v63, 0xffff0000, v103
	v_and_b32_e32 v62, 0xffff0000, v105
	v_pk_mul_f32 v[60:61], v[48:49], v[60:61]
	v_pk_mul_f32 v[68:69], v[48:49], v[70:71]
	v_pk_mul_f32 v[70:71], v[48:49], v[72:73]
	v_pk_mul_f32 v[62:63], v[48:49], v[62:63]
	v_add_f32_e32 v60, v60, v61
	v_add_f32_e32 v61, v68, v69
	v_add_f32_e32 v68, v70, v71
	v_add_f32_e32 v62, v62, v63
	v_fmac_f32_e32 v75, v108, v60
	v_fmac_f32_e32 v79, v109, v61
	v_fmac_f32_e32 v80, v110, v68
	v_fmac_f32_e32 v81, v111, v62
	v_cvt_pk_bf16_f32 v32, v75, v79
	v_cvt_pk_bf16_f32 v33, v80, v81
	v_mul_f32_e32 v70, v79, v79
	global_store_dwordx2 v[30:31], v[32:33], off offset:-3072
	s_nop 0
	v_fmac_f32_e32 v70, v75, v75
	v_fmac_f32_e32 v70, v80, v80
	v_fmac_f32_e32 v70, v81, v81
	v_add_f32_e32 v72, v74, v70
	v_lshlrev_b32_e32 v73, 16, v106
	v_and_b32_e32 v74, 0xffff0000, v106
	v_lshlrev_b32_e32 v82, 16, v107
	v_and_b32_e32 v83, 0xffff0000, v107
	v_lshlrev_b32_e32 v39, 16, v112
	v_lshlrev_b32_e32 v38, 16, v114
	v_and_b32_e32 v61, 0xffff0000, v112
	v_and_b32_e32 v60, 0xffff0000, v114
	v_lshlrev_b32_e32 v71, 16, v113
	v_lshlrev_b32_e32 v70, 16, v115
	v_and_b32_e32 v63, 0xffff0000, v113
	v_and_b32_e32 v62, 0xffff0000, v115
	v_pk_mul_f32 v[38:39], v[48:49], v[38:39]
	v_pk_mul_f32 v[60:61], v[48:49], v[60:61]
	v_pk_mul_f32 v[68:69], v[48:49], v[70:71]
	v_pk_mul_f32 v[62:63], v[48:49], v[62:63]
	v_add_f32_e32 v38, v38, v39
	v_add_f32_e32 v39, v60, v61
	v_add_f32_e32 v60, v68, v69
	v_add_f32_e32 v61, v62, v63
	v_fmac_f32_e32 v73, v116, v38
	v_fmac_f32_e32 v74, v117, v39
	v_fmac_f32_e32 v82, v118, v60
	v_fmac_f32_e32 v83, v119, v61
	v_cvt_pk_bf16_f32 v32, v73, v74
	v_cvt_pk_bf16_f32 v33, v82, v83
	v_mul_f32_e32 v68, v74, v74
	global_store_dwordx2 v[30:31], v[32:33], off offset:-2560
	s_nop 0
	v_fmac_f32_e32 v68, v73, v73
	v_fmac_f32_e32 v68, v82, v82
	v_fmac_f32_e32 v68, v83, v83
	v_add_f32_e32 v70, v72, v68
	v_lshlrev_b32_e32 v71, 16, v120
	v_and_b32_e32 v72, 0xffff0000, v120
	v_lshlrev_b32_e32 v84, 16, v121
	v_and_b32_e32 v85, 0xffff0000, v121
	v_lshlrev_b32_e32 v39, 16, v122
	v_lshlrev_b32_e32 v38, 16, v124
	v_and_b32_e32 v41, 0xffff0000, v122
	v_and_b32_e32 v40, 0xffff0000, v124
	v_lshlrev_b32_e32 v69, 16, v123
	v_lshlrev_b32_e32 v68, 16, v125
	v_and_b32_e32 v61, 0xffff0000, v123
	v_and_b32_e32 v60, 0xffff0000, v125
	v_pk_mul_f32 v[38:39], v[48:49], v[38:39]
	v_pk_mul_f32 v[40:41], v[48:49], v[40:41]
	v_pk_mul_f32 v[62:63], v[48:49], v[68:69]
	v_pk_mul_f32 v[60:61], v[48:49], v[60:61]
	v_add_f32_e32 v38, v38, v39
	v_add_f32_e32 v39, v40, v41
	v_add_f32_e32 v40, v62, v63
	v_add_f32_e32 v41, v60, v61
	v_fmac_f32_e32 v71, v128, v38
	v_fmac_f32_e32 v72, v129, v39
	v_fmac_f32_e32 v84, v130, v40
	v_fmac_f32_e32 v85, v131, v41
	v_cvt_pk_bf16_f32 v32, v71, v72
	v_cvt_pk_bf16_f32 v33, v84, v85
	v_mul_f32_e32 v62, v72, v72
	global_store_dwordx2 v[30:31], v[32:33], off offset:-2048
	s_nop 0
	v_fmac_f32_e32 v62, v71, v71
	v_fmac_f32_e32 v62, v84, v84
	v_fmac_f32_e32 v62, v85, v85
	v_add_f32_e32 v68, v70, v62
	v_lshlrev_b32_e32 v69, 16, v126
	v_and_b32_e32 v70, 0xffff0000, v126
	v_lshlrev_b32_e32 v86, 16, v127
	v_and_b32_e32 v87, 0xffff0000, v127
	v_lshlrev_b32_e32 v39, 16, v132
	v_lshlrev_b32_e32 v38, 16, v134
	v_and_b32_e32 v43, 0xffff0000, v132
	v_and_b32_e32 v42, 0xffff0000, v134
	v_lshlrev_b32_e32 v63, 16, v133
	v_lshlrev_b32_e32 v62, 16, v135
	v_and_b32_e32 v41, 0xffff0000, v133
	v_and_b32_e32 v40, 0xffff0000, v135
	v_pk_mul_f32 v[38:39], v[48:49], v[38:39]
	v_pk_mul_f32 v[42:43], v[48:49], v[42:43]
	v_pk_mul_f32 v[60:61], v[48:49], v[62:63]
	v_pk_mul_f32 v[40:41], v[48:49], v[40:41]
	v_add_f32_e32 v38, v38, v39
	v_add_f32_e32 v39, v42, v43
	v_add_f32_e32 v42, v60, v61
	v_add_f32_e32 v40, v40, v41
	v_fmac_f32_e32 v69, v136, v38
	v_fmac_f32_e32 v70, v137, v39
	v_fmac_f32_e32 v86, v138, v42
	v_fmac_f32_e32 v87, v139, v40
	v_cvt_pk_bf16_f32 v32, v69, v70
	v_cvt_pk_bf16_f32 v33, v86, v87
	v_mul_f32_e32 v60, v70, v70
	global_store_dwordx2 v[30:31], v[32:33], off offset:-1536
	s_nop 0
	v_fmac_f32_e32 v60, v69, v69
	v_fmac_f32_e32 v60, v86, v86
	v_fmac_f32_e32 v60, v87, v87
	v_add_f32_e32 v62, v68, v60
	v_lshlrev_b32_e32 v63, 16, v140
	v_and_b32_e32 v68, 0xffff0000, v140
	v_lshlrev_b32_e32 v88, 16, v141
	v_and_b32_e32 v89, 0xffff0000, v141
	v_lshlrev_b32_e32 v39, 16, v142
	v_lshlrev_b32_e32 v38, 16, v144
	v_and_b32_e32 v45, 0xffff0000, v142
; __device__ __forceinline__ unsigned pk2(float lo, float hi) { unsigned r; asm volatile("v_cvt_pk_bf16_f32 %0, %1, %2" : "=v"(r) : "v"(lo), "v"(hi)); return r; }
; __device__ __forceinline__ f32x4 ldx4(const bf16_t* q) { const u32x2 w = *(const u32x2*)q; f32x4 r; r.x = __uint_as_float(w.x << 16); r.y = __uint_as_float(w.x & 0xffff0000u); r.z = __uint_as_float(w.y << 16); r.w = __uint_as_float(w.y & 0xffff0000u); return r; }
; __device__ __forceinline__ void stx4(bf16_t* q, const f32x4 v) { u32x2 w; w.x = pk2(v.x, v.y); w.y = pk2(v.z, v.w); *(u32x2*)q = w; }
; template <bool FINAL>
; __device__ __forceinline__ void ph_moe_combine(const P& p, int l, int row0, int gw, int nw, int lane) {
;     ...
;     for (int j = 0; j < 8; ++j) { const int c = (lane + 64 * j) * 4;
;       const u32x2 a = __builtin_nontemporal_load((const u32x2*)(y0 + c)), b = __builtin_nontemporal_load((const u32x2*)(y1 + c)); f32x4 xv = ldx4(xr + c); const f32x4 g = *(const f32x4*)(gt + c);
;       xv.x += g.x * (w0 * __uint_as_float(a.x << 16) + w1 * __uint_as_float(b.x << 16));
;       xv.y += g.y * (w0 * __uint_as_float(a.x & 0xffff0000u) + w1 * __uint_as_float(b.x & 0xffff0000u));
;       xv.z += g.z * (w0 * __uint_as_float(a.y << 16) + w1 * __uint_as_float(b.y << 16));
;       xv.w += g.w * (w0 * __uint_as_float(a.y & 0xffff0000u) + w1 * __uint_as_float(b.y & 0xffff0000u));
;       v[j] = xv; ss += xv.x * xv.x + xv.y * xv.y + xv.z * xv.z + xv.w * xv.w;
;       if (!FINAL) stx4(xr + c, xv); }
;     if (!FINAL) {
;       const float rs = rsqrtf(wave_sum(ss) * (1.f / DM) + EPS);
;       const float* g1 = p.n1 + (l + 1) * DM; const float* md = WSP(float, WS_MOD) + ((size_t)(l + 1) * 2 + (r < CTXL ? 1 : 0)) * MODW;
;       bf16_t* o = WSP(bf16_t, WS_HN) + (size_t)r * DM;
; #pragma unroll
;       for (int j = 0; j < 8; ++j) { const int c = (lane + 64 * j) * 4; const f32x4 gg = *(const f32x4*)(g1 + c), sh = *(const f32x4*)(md + c), sc = *(const f32x4*)(md + DM + c);
;         u32x2 w2; w2.x = pk2(v[j].x * rs * gg.x * (1.f + sc.x) + sh.x, v[j].y * rs * gg.y * (1.f + sc.y) + sh.y); w2.y = pk2(v[j].z * rs * gg.z * (1.f + sc.z) + sh.z, v[j].w * rs * gg.w * (1.f + sc.w) + sh.w);
;         *(u32x2*)(o + c) = w2; }
	v_and_b32_e32 v44, 0xffff0000, v144
	v_lshlrev_b32_e32 v61, 16, v143
	v_lshlrev_b32_e32 v60, 16, v145
	v_and_b32_e32 v41, 0xffff0000, v143
	v_and_b32_e32 v40, 0xffff0000, v145
	v_pk_mul_f32 v[38:39], v[48:49], v[38:39]
	v_pk_mul_f32 v[42:43], v[48:49], v[44:45]
	v_pk_mul_f32 v[44:45], v[48:49], v[60:61]
	v_pk_mul_f32 v[40:41], v[48:49], v[40:41]
	v_add_f32_e32 v38, v38, v39
	v_add_f32_e32 v39, v42, v43
	v_add_f32_e32 v42, v44, v45
	v_add_f32_e32 v40, v40, v41
	v_fmac_f32_e32 v63, v148, v38
	v_fmac_f32_e32 v68, v149, v39
	v_fmac_f32_e32 v88, v150, v42
	v_fmac_f32_e32 v89, v151, v40
	v_cvt_pk_bf16_f32 v32, v63, v68
	v_cvt_pk_bf16_f32 v33, v88, v89
	v_mul_f32_e32 v44, v68, v68
	global_store_dwordx2 v[30:31], v[32:33], off offset:-1024
	s_nop 0
	v_fmac_f32_e32 v44, v63, v63
	v_fmac_f32_e32 v44, v88, v88
	v_fmac_f32_e32 v44, v89, v89
	v_add_f32_e32 v60, v62, v44
	v_lshlrev_b32_e32 v61, 16, v146
	v_and_b32_e32 v62, 0xffff0000, v146
	v_lshlrev_b32_e32 v90, 16, v147
	v_and_b32_e32 v91, 0xffff0000, v147
	v_lshlrev_b32_e32 v39, 16, v152
	v_lshlrev_b32_e32 v38, 16, v154
	v_and_b32_e32 v45, 0xffff0000, v152
	v_and_b32_e32 v44, 0xffff0000, v154
	v_lshlrev_b32_e32 v47, 16, v153
	v_lshlrev_b32_e32 v46, 16, v155
	v_and_b32_e32 v41, 0xffff0000, v153
	v_and_b32_e32 v40, 0xffff0000, v155
	v_pk_mul_f32 v[38:39], v[48:49], v[38:39]
	v_pk_mul_f32 v[42:43], v[48:49], v[44:45]
	v_pk_mul_f32 v[44:45], v[48:49], v[46:47]
	v_pk_mul_f32 v[40:41], v[48:49], v[40:41]
	v_add_f32_e32 v38, v38, v39
	v_add_f32_e32 v39, v42, v43
	v_add_f32_e32 v42, v44, v45
	v_add_f32_e32 v40, v40, v41
	v_fmac_f32_e32 v61, v156, v38
	v_fmac_f32_e32 v62, v157, v39
	v_fmac_f32_e32 v90, v158, v42
	v_fmac_f32_e32 v91, v159, v40
	v_cvt_pk_bf16_f32 v32, v61, v62
	v_cvt_pk_bf16_f32 v33, v90, v91
	v_mul_f32_e32 v44, v62, v62
	global_store_dwordx2 v[30:31], v[32:33], off offset:-512
	s_nop 0
	v_fmac_f32_e32 v44, v61, v61
	v_fmac_f32_e32 v44, v90, v90
	v_fmac_f32_e32 v44, v91, v91
	v_add_f32_e32 v52, v60, v44
	v_lshlrev_b32_e32 v53, 16, v160
	v_and_b32_e32 v60, 0xffff0000, v160
	v_lshlrev_b32_e32 v64, 16, v161
	v_and_b32_e32 v65, 0xffff0000, v161
	v_lshlrev_b32_e32 v39, 16, v162
	v_lshlrev_b32_e32 v38, 16, v164
	v_and_b32_e32 v45, 0xffff0000, v162
	v_and_b32_e32 v44, 0xffff0000, v164
	v_lshlrev_b32_e32 v47, 16, v163
	v_lshlrev_b32_e32 v46, 16, v165
	v_and_b32_e32 v41, 0xffff0000, v163
	v_and_b32_e32 v40, 0xffff0000, v165
	v_pk_mul_f32 v[38:39], v[48:49], v[38:39]
	v_pk_mul_f32 v[42:43], v[48:49], v[44:45]
	v_pk_mul_f32 v[44:45], v[48:49], v[46:47]
	v_pk_mul_f32 v[40:41], v[48:49], v[40:41]
	v_add_f32_e32 v38, v38, v39
	v_add_f32_e32 v39, v42, v43
	v_add_f32_e32 v42, v44, v45
	v_add_f32_e32 v40, v40, v41
	v_fmac_f32_e32 v53, v168, v38
	v_fmac_f32_e32 v60, v169, v39
	v_fmac_f32_e32 v64, v170, v42
	v_fmac_f32_e32 v65, v171, v40
	v_cvt_pk_bf16_f32 v32, v53, v60
	v_cvt_pk_bf16_f32 v33, v64, v65
	global_store_dwordx2 v[30:31], v[32:33], off
	global_load_dwordx4 v[108:111], v[4:5], off
	global_load_dwordx4 v[116:119], v22, s[38:39] offset:1024
	global_load_dwordx4 v[128:131], v22, s[34:35] offset:1024
	global_load_dwordx4 v[136:139], v[6:7], off
	global_load_dwordx4 v[148:151], v22, s[38:39] offset:2048
	global_load_dwordx4 v[156:159], v22, s[34:35] offset:2048
	global_load_dwordx4 v[168:171], v[8:9], off
	global_load_dwordx4 v[244:247], v22, s[38:39] offset:3072
	global_load_dwordx4 v[248:251], v22, s[34:35] offset:3072
	s_nop 0
	v_mul_f32_e32 v34, v60, v60
	v_fmac_f32_e32 v34, v53, v53
	v_fmac_f32_e32 v34, v64, v64
	v_fmac_f32_e32 v34, v65, v65
	v_add_f32_e32 v34, v52, v34
	s_nop 1
	v_add_f32_dpp v34, v34, v34 quad_perm:[1,0,3,2] row_mask:0xf bank_mask:0xf bound_ctrl:1
	s_nop 1
	v_add_f32_dpp v34, v34, v34 quad_perm:[2,3,0,1] row_mask:0xf bank_mask:0xf bound_ctrl:1
	s_nop 1
	v_add_f32_dpp v34, v34, v34 row_half_mirror row_mask:0xf bank_mask:0xf bound_ctrl:1
	s_nop 1
	v_add_f32_dpp v34, v34, v34 row_mirror row_mask:0xf bank_mask:0xf bound_ctrl:1
	v_mov_b32_e32 v35, v34
	s_nop 1
	v_permlane16_swap_b32_e32 v34, v35
	v_add_f32_e32 v34, v34, v35
	v_mov_b32_e32 v35, v34
	s_nop 1
	v_permlane32_swap_b32_e32 v34, v35
	v_add_f32_e32 v34, v34, v35
	v_fmamk_f32 v34, v34, 0x3a000000, v178
	v_mul_f32_e32 v35, 0x4b800000, v34
	v_cmp_gt_f32_e32 vcc, s37, v34
	s_nop 1
	v_cndmask_b32_e32 v34, v34, v35, vcc
	v_rsq_f32_e32 v34, v34
	s_nop 0
	v_mul_f32_e32 v35, 0x45800000, v34
	v_cndmask_b32_e32 v46, v34, v35, vcc
	v_mul_f32_e32 v34, v59, v46
	v_mul_f32_e32 v35, v76, v46
	v_mul_f32_e32 v47, v77, v46
	v_mul_f32_e32 v48, v78, v46
	v_mul_f32_e32 v49, v75, v46
	v_mul_f32_e32 v52, v79, v46
	v_mul_f32_e32 v56, v80, v46
	v_mul_f32_e32 v57, v81, v46
	v_mul_f32_e32 v30, v172, v34
	v_add_f32_e32 v34, 1.0, v180
	v_mul_f32_e32 v31, v173, v35
	v_add_f32_e32 v35, 1.0, v181
	v_mul_f32_e32 v32, v174, v47
	v_add_f32_e32 v38, 1.0, v182
	v_mul_f32_e32 v33, v175, v48
	v_add_f32_e32 v39, 1.0, v183
	v_fma_f32 v30, v34, v30, v184
; __device__ __forceinline__ unsigned pk2(float lo, float hi) { unsigned r; asm volatile("v_cvt_pk_bf16_f32 %0, %1, %2" : "=v"(r) : "v"(lo), "v"(hi)); return r; }
; template <bool FINAL>
; __device__ __forceinline__ void ph_moe_combine(const P& p, int l, int row0, int gw, int nw, int lane) {
;     ...
;     if (!FINAL) {
;       const float rs = rsqrtf(wave_sum(ss) * (1.f / DM) + EPS);
;       const float* g1 = p.n1 + (l + 1) * DM; const float* md = WSP(float, WS_MOD) + ((size_t)(l + 1) * 2 + (r < CTXL ? 1 : 0)) * MODW;
;       bf16_t* o = WSP(bf16_t, WS_HN) + (size_t)r * DM;
; #pragma unroll
;       for (int j = 0; j < 8; ++j) { const int c = (lane + 64 * j) * 4; const f32x4 gg = *(const f32x4*)(g1 + c), sh = *(const f32x4*)(md + c), sc = *(const f32x4*)(md + DM + c);
;         u32x2 w2; w2.x = pk2(v[j].x * rs * gg.x * (1.f + sc.x) + sh.x, v[j].y * rs * gg.y * (1.f + sc.y) + sh.y); w2.y = pk2(v[j].z * rs * gg.z * (1.f + sc.z) + sh.z, v[j].w * rs * gg.w * (1.f + sc.w) + sh.w);
;         *(u32x2*)(o + c) = w2; }
;     }
	v_fma_f32 v31, v35, v31, v185
	v_fma_f32 v32, v38, v32, v186
	v_fmac_f32_e32 v187, v39, v33
	v_cvt_pk_bf16_f32 v30, v30, v31
	v_cvt_pk_bf16_f32 v31, v32, v187
	global_store_dwordx2 v[12:13], v[30:31], off offset:-3584
	s_nop 0
	v_mul_f32_e32 v47, v73, v46
	v_mul_f32_e32 v48, v74, v46
	v_mul_f32_e32 v30, v188, v49
	v_add_f32_e32 v34, 1.0, v192
	v_mul_f32_e32 v31, v189, v52
	v_add_f32_e32 v35, 1.0, v193
	v_mul_f32_e32 v32, v190, v56
	v_add_f32_e32 v38, 1.0, v194
	v_mul_f32_e32 v33, v191, v57
	v_add_f32_e32 v39, 1.0, v195
	v_fma_f32 v30, v34, v30, v196
	v_fma_f32 v31, v35, v31, v197
	v_fma_f32 v32, v38, v32, v198
	v_fmac_f32_e32 v199, v39, v33
	v_cvt_pk_bf16_f32 v30, v30, v31
	v_cvt_pk_bf16_f32 v31, v32, v199
	global_store_dwordx2 v[12:13], v[30:31], off offset:-3072
	s_nop 0
	v_mul_f32_e32 v49, v82, v46
	v_mul_f32_e32 v50, v83, v46
	v_lshl_add_u64 v[34:35], s[38:39], 0, v[20:21]
	v_mul_f32_e32 v30, v47, v200
	v_add_f32_e32 v38, 1.0, v204
	v_mul_f32_e32 v31, v48, v201
	v_add_f32_e32 v39, 1.0, v205
	v_mul_f32_e32 v32, v49, v202
	v_add_f32_e32 v40, 1.0, v206
	v_mul_f32_e32 v33, v50, v203
	v_add_f32_e32 v41, 1.0, v207
	v_fma_f32 v30, v30, v38, v208
	v_fma_f32 v31, v31, v39, v209
	v_fma_f32 v32, v32, v40, v210
	v_fmac_f32_e32 v211, v33, v41
	v_cvt_pk_bf16_f32 v30, v30, v31
	v_cvt_pk_bf16_f32 v31, v32, v211
	global_store_dwordx2 v[12:13], v[30:31], off offset:-2560
	s_nop 0
	s_nop 0
	v_mul_f32_e32 v47, v71, v46
	v_mul_f32_e32 v48, v72, v46
	v_mul_f32_e32 v49, v84, v46
	v_mul_f32_e32 v50, v85, v46
	v_lshl_add_u64 v[42:43], s[34:35], 0, v[22:23]
	v_lshl_add_u64 v[44:45], s[38:39], 0, v[22:23]
	v_mul_f32_e32 v30, v47, v212
	v_add_f32_e32 v38, 1.0, v224
	v_mul_f32_e32 v31, v48, v213
	v_add_f32_e32 v39, 1.0, v225
	v_mul_f32_e32 v32, v49, v214
	v_add_f32_e32 v40, 1.0, v226
	v_mul_f32_e32 v33, v50, v215
	v_add_f32_e32 v41, 1.0, v227
	v_fma_f32 v30, v30, v38, v228
	v_fma_f32 v31, v31, v39, v229
	v_fma_f32 v32, v32, v40, v230
	v_fmac_f32_e32 v231, v33, v41
	v_cvt_pk_bf16_f32 v30, v30, v31
	v_cvt_pk_bf16_f32 v31, v32, v231
	global_store_dwordx2 v[12:13], v[30:31], off offset:-2048
	s_nop 0
	v_mul_f32_e32 v47, v69, v46
	v_mul_f32_e32 v48, v70, v46
	v_mul_f32_e32 v49, v86, v46
	v_mul_f32_e32 v50, v87, v46
	v_lshl_add_u64 v[42:43], s[34:35], 0, v[24:25]
	v_lshl_add_u64 v[44:45], s[38:39], 0, v[24:25]
	v_mul_f32_e32 v30, v47, v232
	v_add_f32_e32 v34, 1.0, v236
	v_mul_f32_e32 v31, v48, v233
	v_add_f32_e32 v35, 1.0, v237
	v_mul_f32_e32 v32, v49, v234
	v_add_f32_e32 v36, 1.0, v238
	v_mul_f32_e32 v33, v50, v235
	v_add_f32_e32 v37, 1.0, v239
	v_fma_f32 v30, v30, v34, v240
	v_fma_f32 v31, v31, v35, v241
	v_fma_f32 v32, v32, v36, v242
	v_fmac_f32_e32 v243, v33, v37
	v_cvt_pk_bf16_f32 v30, v30, v31
	v_cvt_pk_bf16_f32 v31, v32, v243
	global_store_dwordx2 v[12:13], v[30:31], off offset:-1536
	s_nop 0
	v_mul_f32_e32 v47, v63, v46
	v_mul_f32_e32 v48, v68, v46
	v_mul_f32_e32 v49, v88, v46
	v_mul_f32_e32 v50, v89, v46
	v_lshl_add_u64 v[42:43], s[34:35], 0, v[26:27]
	v_lshl_add_u64 v[44:45], s[38:39], 0, v[26:27]
	s_waitcnt vmcnt(5)
	v_mul_f32_e32 v30, v47, v108
	v_add_f32_e32 v34, 1.0, v116
	v_mul_f32_e32 v31, v48, v109
	v_add_f32_e32 v35, 1.0, v117
	v_mul_f32_e32 v32, v49, v110
	v_add_f32_e32 v36, 1.0, v118
	v_mul_f32_e32 v33, v50, v111
	v_add_f32_e32 v37, 1.0, v119
	v_fma_f32 v30, v30, v34, v128
	v_fma_f32 v31, v31, v35, v129
	v_fma_f32 v32, v32, v36, v130
	v_fmac_f32_e32 v131, v33, v37
	v_cvt_pk_bf16_f32 v30, v30, v31
	v_cvt_pk_bf16_f32 v31, v32, v131
	global_store_dwordx2 v[12:13], v[30:31], off offset:-1024
	s_nop 0
	v_mul_f32_e32 v47, v61, v46
	v_mul_f32_e32 v48, v62, v46
	v_mul_f32_e32 v49, v90, v46
	v_mul_f32_e32 v50, v91, v46
	v_lshl_add_u64 v[42:43], s[34:35], 0, v[28:29]
	v_lshl_add_u64 v[44:45], s[38:39], 0, v[28:29]
	v_mul_f32_e32 v30, v47, v136
	v_add_f32_e32 v34, 1.0, v148
	v_mul_f32_e32 v31, v48, v137
	v_add_f32_e32 v35, 1.0, v149
	v_mul_f32_e32 v32, v49, v138
	v_add_f32_e32 v36, 1.0, v150
	v_mul_f32_e32 v33, v50, v139
	v_add_f32_e32 v37, 1.0, v151
	v_fma_f32 v30, v30, v34, v156
	v_fma_f32 v31, v31, v35, v157
	v_fma_f32 v32, v32, v36, v158
	v_fmac_f32_e32 v159, v33, v37
	v_cvt_pk_bf16_f32 v30, v30, v31
	v_cvt_pk_bf16_f32 v31, v32, v159
	global_store_dwordx2 v[12:13], v[30:31], off offset:-512
	s_nop 0
	v_mul_f32_e32 v42, v53, v46
	v_mul_f32_e32 v43, v60, v46
	v_mul_f32_e32 v44, v64, v46
	v_mul_f32_e32 v45, v65, v46
	v_mul_f32_e32 v30, v42, v168
	v_add_f32_e32 v34, 1.0, v244
	v_mul_f32_e32 v31, v43, v169
	v_add_f32_e32 v35, 1.0, v245
	v_mul_f32_e32 v32, v44, v170
	v_add_f32_e32 v36, 1.0, v246
	v_mul_f32_e32 v33, v45, v171
	v_add_f32_e32 v37, 1.0, v247
	v_fma_f32 v30, v30, v34, v248
	v_fma_f32 v31, v31, v35, v249
	v_fma_f32 v32, v32, v36, v250
	v_fmac_f32_e32 v251, v33, v37
	v_cvt_pk_bf16_f32 v30, v30, v31
	v_cvt_pk_bf16_f32 v31, v32, v251
	global_store_dwordx2 v[12:13], v[30:31], off
	v_lshl_add_u64 v[12:13], v[12:13], 0, s[20:21]
	s_cbranch_scc1 .LBB0_1421
